# attention loop LDS fragment lookahead 8 instead of 7
# speedup vs baseline: 1.0041x; 1.0041x over previous
.LBB0_733:
	s_or_b64 exec, exec, s[8:9]
	s_movk_i32 s4, 0xf0
	s_cmp_lg_u32 0, -1
	v_lshlrev_b32_e32 v39, 8, v141
	v_bitop3_b32 v80, v142, s4, v136 bitop3:0x48
	s_cselect_b32 s10, 0, 0
	v_cvt_pk_bf16_f32 v96, v134, v135
	v_cvt_pk_bf16_f32 v97, v132, v133
	v_cvt_pk_bf16_f32 v98, v130, v131
	v_cvt_pk_bf16_f32 v99, v128, v129
	v_cvt_pk_bf16_f32 v100, v126, v127
	v_cvt_pk_bf16_f32 v101, v124, v125
	v_cvt_pk_bf16_f32 v102, v122, v123
	v_cvt_pk_bf16_f32 v103, v120, v121
	v_cvt_pk_bf16_f32 v104, v70, v71
	v_cvt_pk_bf16_f32 v105, v74, v75
	v_cvt_pk_bf16_f32 v106, v64, v65
	v_cvt_pk_bf16_f32 v107, v68, v69
	v_cvt_pk_bf16_f32 v108, v60, v61
	v_cvt_pk_bf16_f32 v109, v66, v67
	v_cvt_pk_bf16_f32 v110, v56, v57
	v_cvt_pk_bf16_f32 v111, v58, v59
	v_cvt_pk_bf16_f32 v112, v112, v113
	v_cvt_pk_bf16_f32 v113, v118, v119
	v_cvt_pk_bf16_f32 v114, v114, v115
	v_cvt_pk_bf16_f32 v115, v116, v117
	v_cvt_pk_bf16_f32 v116, v78, v79
	v_cvt_pk_bf16_f32 v117, v76, v77
	v_cvt_pk_bf16_f32 v118, v72, v73
	v_cvt_pk_bf16_f32 v119, v62, v63
	v_cvt_pk_bf16_f32 v120, v52, v53
	v_cvt_pk_bf16_f32 v121, v54, v55
	v_cvt_pk_bf16_f32 v122, v46, v47
	v_cvt_pk_bf16_f32 v123, v50, v51
	v_cvt_pk_bf16_f32 v124, v44, v45
	v_cvt_pk_bf16_f32 v125, v48, v49
	v_cvt_pk_bf16_f32 v126, v40, v41
	v_cvt_pk_bf16_f32 v127, v42, v43
	v_readlane_b32 s100, v250, 8
	v_mbcnt_lo_u32_b32 v68, -1, 0
	v_mbcnt_hi_u32_b32 v68, -1, v68
	s_nop 1
	v_add_u32_e32 v69, s100, v68
	v_lshrrev_b32_e32 v70, 3, v69
	v_and_b32_e32 v71, 7, v69
	v_lshrrev_b32_e32 v72, 2, v71
	v_bfe_u32 v73, v71, 1, 1
	v_and_b32_e32 v74, 1, v71
	v_lshlrev_b32_e32 v74, 1, v74
	v_lshl_add_u32 v75, v72, 2, v74
	v_bfe_u32 v76, v70, 1, 3
	v_xor_b32_e32 v77, v75, v76
	v_add_u32_e32 v78, 1, v75
	v_xor_b32_e32 v78, v78, v76
	v_lshlrev_b32_e32 v79, 7, v70
	v_lshl_add_u32 v79, v73, 3, v79
	v_lshl_add_u32 v64, v77, 4, v79
	v_lshl_add_u32 v65, v78, 4, v79
	v_add_u32_e32 v66, 0x2000, v64
	v_add_u32_e32 v67, 0x2000, v65
	v_or_b32_e32 v81, v39, v80
	s_add_i32 s15, s10, 0x10000
	v_and_b32_e32 v82, 6, v137
	v_lshrrev_b32_e32 v84, 4, v136
	s_waitcnt vmcnt(0)
	s_waitcnt vmcnt(0)
	s_add_i32 s11, s10, 0x12000
	v_lshl_add_u32 v83, v139, 7, s10
	v_bitop3_b32 v85, v84, v82, 7 bitop3:0x6c
	v_and_b32_e32 v86, 8, v138
	v_or_b32_e32 v82, 1, v82
	v_add_u32_e32 v225, s15, v81
	s_waitcnt vmcnt(4)
	ds_write_b128 v225, v[24:27] offset:0
	v_lshlrev_b32_e32 v85, 4, v85
	v_add_u32_e32 v87, v83, v86
	v_bitop3_b32 v82, v84, v82, 7 bitop3:0x6c
	v_add3_u32 v226, v80, s11, v39
	ds_write_b128 v226, v[28:31] offset:0
	v_lshlrev_b32_e32 v82, 4, v82
	v_add_u32_e32 v227, v87, v85
	ds_write_b64 v64, v[12:13] offset:0
	v_lshrrev_b32_e32 v32, 5, v136
	v_add_u32_e32 v83, 0x2000, v83
	v_or_b32_e32 v84, v85, v86
	v_add_u32_e32 v228, v87, v82
	ds_write_b64 v65, v[14:15] offset:0
	v_xor_b32_e32 v32, v32, v137
	v_or_b32_e32 v86, v82, v86
	v_add_u32_e32 v229, v84, v83
	ds_write_b64 v66, v[4:5] offset:0
	v_lshlrev_b32_e32 v32, 4, v32
	v_add_u32_e32 v184, v86, v83
	ds_write_b64 v67, v[6:7] offset:0
	v_lshlrev_b32_e32 v33, 8, v143
	v_and_b32_e32 v32, 16, v32
	v_bfe_u32 v35, v137, 1, 3
	s_waitcnt vmcnt(4)
	ds_write_b128 v225, v[20:23] offset:0x4000
	v_lshlrev_b32_e32 v36, 5, v35
	v_add3_u32 v32, v33, s15, v32
	s_movk_i32 s16, 0x60
	ds_write_b128 v226, v[16:19] offset:0x4000
	v_xad_u32 v204, v36, s16, v32
	s_movk_i32 s16, 0x80
	ds_write_b64 v64, v[8:9] offset:0x4000
	v_xad_u32 v205, v36, s16, v32
	s_movk_i32 s16, 0xa0
	ds_write_b64 v65, v[10:11] offset:0x4000
	s_add_u32 s8, s6, 0x100
	v_xad_u32 v206, v36, s16, v32
	s_movk_i32 s16, 0xc0
	ds_write_b64 v66, v[0:1] offset:0x4000
	s_addc_u32 s9, s7, 0
	v_xad_u32 v207, v36, s16, v32
	s_movk_i32 s16, 0xe0
	ds_write_b64 v67, v[2:3] offset:0x4000
	v_add_u32_e32 v201, v32, v36
	v_xad_u32 v202, v36, 32, v32
	v_xad_u32 v203, v36, 64, v32
	v_xad_u32 v208, v36, s16, v32
	v_lshl_add_u32 v32, v143, 7, s10
	s_add_u32 s10, s78, 0x20000
	global_load_dwordx4 v[132:135], v198, s[8:9]
	s_addc_u32 s11, s79, 0
	global_load_dwordx4 v[128:131], v199, s[8:9]
	v_lshrrev_b32_e32 v34, 1, v137
	global_load_dwordx4 v[136:139], v196, s[10:11]
	s_add_u32 s6, s6, 0x180
	v_bitop3_b32 v34, v140, v34, 7 bitop3:0x78
	v_bitop3_b32 v37, v140, v35, 2 bitop3:0x36
	v_bitop3_b32 v38, v140, v35, 4 bitop3:0x36
	v_bitop3_b32 v35, v140, v35, 6 bitop3:0x36
	global_load_dwordx4 v[140:143], v197, s[10:11]
	s_addc_u32 s7, s7, 0
	s_add_u32 s8, s78, 0x30000
	global_load_dwordx4 v[148:151], v198, s[6:7]
	s_addc_u32 s9, s79, 0
	global_load_dwordx4 v[144:147], v199, s[6:7]
	global_load_dwordx4 v[152:155], v196, s[8:9]
	s_add_u32 s10, s13, s14
	global_load_dwordx4 v[156:159], v197, s[8:9]
	s_addc_u32 s11, s12, 0
	s_add_u32 s12, s41, s30
	v_mov_b32_e32 v0, 0
	s_mov_b32 s4, 0
	v_lshl_add_u32 v209, v34, 4, v32
	v_lshl_add_u32 v210, v37, 4, v32
	v_lshl_add_u32 v211, v38, 4, v32
	v_lshl_add_u32 v224, v35, 4, v32
	s_addc_u32 s13, 0, s31
	v_mov_b32_e32 v1, v0
	v_mov_b32_e32 v2, v0
	v_mov_b32_e32 v3, v0
	v_mov_b32_e32 v4, v0
	v_mov_b32_e32 v5, v0
	v_mov_b32_e32 v6, v0
	v_mov_b32_e32 v7, v0
	v_mov_b32_e32 v8, v0
	v_mov_b32_e32 v9, v0
	v_mov_b32_e32 v10, v0
	v_mov_b32_e32 v11, v0
	v_mov_b32_e32 v12, v0
	v_mov_b32_e32 v13, v0
	v_mov_b32_e32 v14, v0
	v_mov_b32_e32 v15, v0
	v_mov_b32_e32 v16, v0
	v_mov_b32_e32 v17, v0
	v_mov_b32_e32 v18, v0
	v_mov_b32_e32 v19, v0
	v_mov_b32_e32 v20, v0
	v_mov_b32_e32 v21, v0
	v_mov_b32_e32 v22, v0
	v_mov_b32_e32 v23, v0
	v_mov_b32_e32 v24, v0
	v_mov_b32_e32 v25, v0
	v_mov_b32_e32 v26, v0
	v_mov_b32_e32 v27, v0
	v_mov_b32_e32 v28, v0
	v_mov_b32_e32 v29, v0
	v_mov_b32_e32 v30, v0
	v_mov_b32_e32 v31, v0
	v_mov_b32_e32 v32, v0
	v_mov_b32_e32 v33, v0
	v_mov_b32_e32 v34, v0
	v_mov_b32_e32 v35, v0
	v_mov_b32_e32 v36, v0
	v_mov_b32_e32 v37, v0
	v_mov_b32_e32 v38, v0
	v_mov_b32_e32 v39, v0
	v_mov_b32_e32 v40, v0
	v_mov_b32_e32 v41, v0
	v_mov_b32_e32 v42, v0
	v_mov_b32_e32 v43, v0
	v_mov_b32_e32 v44, v0
	v_mov_b32_e32 v45, v0
	v_mov_b32_e32 v46, v0
	v_mov_b32_e32 v47, v0
	v_mov_b32_e32 v48, v0
	v_mov_b32_e32 v49, v0
	v_mov_b32_e32 v50, v0
	v_mov_b32_e32 v51, v0
	v_mov_b32_e32 v52, v0
	v_mov_b32_e32 v53, v0
	v_mov_b32_e32 v54, v0
	v_mov_b32_e32 v55, v0
	v_mov_b32_e32 v56, v0
	v_mov_b32_e32 v57, v0
	v_mov_b32_e32 v58, v0
	v_mov_b32_e32 v59, v0
	v_mov_b32_e32 v60, v0
	v_mov_b32_e32 v61, v0
	v_mov_b32_e32 v62, v0
	v_mov_b32_e32 v63, v0
	v_mov_b32_e32 v160, v0
	v_mov_b32_e32 v161, v0
	v_mov_b32_e32 v227, v64
	v_mov_b32_e32 v228, v65
	v_mov_b32_e32 v229, v66
	v_mov_b32_e32 v184, v67
	v_readlane_b32 s100, v250, 8
	v_mbcnt_lo_u32_b32 v68, -1, 0
	v_mbcnt_hi_u32_b32 v68, -1, v68
	v_and_b32_e32 v69, 15, v68
	v_lshrrev_b32_e32 v70, 4, v68
	v_lshlrev_b32_e32 v72, 8, v69
	v_add_u32_e32 v72, 0x10000, v72
	v_add_u32_e32 v71, 0, v70
	v_xor_b32_e32 v71, v71, v69
	v_lshl_add_u32 v201, v71, 4, v72
	v_add_u32_e32 v71, 4, v70
	v_xor_b32_e32 v71, v71, v69
	v_lshl_add_u32 v202, v71, 4, v72
	v_add_u32_e32 v71, 8, v70
	v_xor_b32_e32 v71, v71, v69
	v_lshl_add_u32 v203, v71, 4, v72
	v_add_u32_e32 v71, 12, v70
	v_xor_b32_e32 v71, v71, v69
	v_lshl_add_u32 v246, v71, 4, v72
	v_bfe_u32 v73, v69, 1, 3
	v_lshlrev_b32_e32 v76, 7, v69
	v_add_u32_e32 v71, 0, v70
	v_xor_b32_e32 v71, v71, v73
	v_lshl_add_u32 v209, v71, 4, v76
	v_add_u32_e32 v71, 4, v70
	v_xor_b32_e32 v71, v71, v73
	v_lshl_add_u32 v210, v71, 4, v76
	s_lshl_b32 s101, s100, 7
	s_add_u32 s101, s101, 0x8000
	s_cmpk_ge_u32 s100, 0x100
	s_cselect_b32 s6, 0x8000, 0
	s_add_u32 s101, s101, s6
	v_and_b32_e32 v74, 31, v68
	v_lshrrev_b32_e32 v75, 5, v68
	v_lshlrev_b32_e32 v74, 8, v74
	v_lshl_add_u32 v74, v75, 4, v74
	v_add_u32_e32 v74, s101, v74
	v_lshlrev_b32_e32 v75, 8, v69
	v_lshl_add_u32 v75, v70, 4, v75
	v_add_u32_e32 v75, s101, v75
	ds_write_b128 v74, v[96:99] offset:0
	ds_write_b128 v74, v[100:103] offset:32
	ds_write_b128 v74, v[104:107] offset:64
	ds_write_b128 v74, v[108:111] offset:96
	ds_write_b128 v74, v[112:115] offset:128
	ds_write_b128 v74, v[116:119] offset:160
	ds_write_b128 v74, v[120:123] offset:192
	ds_write_b128 v74, v[124:127] offset:224
	s_waitcnt lgkmcnt(0)
	ds_read_b128 v[96:99], v75 offset:0
	ds_read_b128 v[100:103], v75 offset:64
	ds_read_b128 v[104:107], v75 offset:128
	ds_read_b128 v[108:111], v75 offset:192
	ds_read_b128 v[112:115], v75 offset:4096
	ds_read_b128 v[116:119], v75 offset:4160
	ds_read_b128 v[120:123], v75 offset:4224
	ds_read_b128 v[124:127], v75 offset:4288
	s_waitcnt vmcnt(0)
	s_waitcnt lgkmcnt(0)
	s_barrier
	ds_write_b128 v225, v[136:139] offset:32768
	ds_write_b128 v226, v[140:143] offset:32768
	s_add_u32 s15, s22, s12
	s_addc_u32 s14, s23, s13
	s_add_u32 s6, s15, 0x23a40000
	s_addc_u32 s7, s14, 0
	s_waitcnt lgkmcnt(0)
	global_load_dwordx4 v[136:139], v196, s[6:7]
	global_load_dwordx4 v[140:143], v197, s[6:7]
	v_mov_b32_e32 v194, 0
	v_mov_b32_e32 v195, 0
	s_barrier
	s_cmpk_ge_u32 s100, 0x100
	s_cselect_b32 s100, 1, 0
	ds_read_b128 v[160:163], v201 offset:0
	ds_read_b128 v[164:167], v202 offset:0
	ds_read_b128 v[168:171], v203 offset:0
	ds_read_b128 v[172:175], v246 offset:0
	ds_read_b128 v[176:179], v201 offset:4096
	ds_read_b128 v[180:183], v202 offset:4096
	ds_read_b128 v[230:233], v203 offset:4096
	s_waitcnt lgkmcnt(6)
	v_mfma_f32_16x16x32_bf16 v[64:67], v[160:163], v[96:99], 0
	v_mfma_f32_16x16x32_bf16 v[68:71], v[160:163], v[112:115], 0
	ds_read_b128 v[234:237], v246 offset:4096
	s_waitcnt lgkmcnt(6)
	v_mfma_f32_16x16x32_bf16 v[68:71], v[164:167], v[116:119], v[68:71]
	v_mfma_f32_16x16x32_bf16 v[64:67], v[164:167], v[100:103], v[64:67]
	ds_read_b128 v[160:163], v201 offset:8192
	s_waitcnt lgkmcnt(6)
	v_mfma_f32_16x16x32_bf16 v[64:67], v[168:171], v[104:107], v[64:67]
	v_mfma_f32_16x16x32_bf16 v[68:71], v[168:171], v[120:123], v[68:71]
	ds_read_b128 v[164:167], v202 offset:8192
	s_waitcnt lgkmcnt(6)
	v_mfma_f32_16x16x32_bf16 v[68:71], v[172:175], v[124:127], v[68:71]
	v_mfma_f32_16x16x32_bf16 v[64:67], v[172:175], v[108:111], v[64:67]
	ds_read_b128 v[168:171], v203 offset:8192
	s_waitcnt lgkmcnt(6)
	v_mfma_f32_16x16x32_bf16 v[72:75], v[176:179], v[96:99], 0
	s_nop 7
	s_nop 1
	v_exp_f32_e32 v64, v64
	v_mfma_f32_16x16x32_bf16 v[76:79], v[176:179], v[112:115], 0
	v_exp_f32_e32 v68, v68
	ds_read_b128 v[172:175], v246 offset:8192
	s_waitcnt lgkmcnt(6)
	v_mfma_f32_16x16x32_bf16 v[76:79], v[180:183], v[116:119], v[76:79]
	v_exp_f32_e32 v65, v65
	v_exp_f32_e32 v69, v69
	v_mfma_f32_16x16x32_bf16 v[72:75], v[180:183], v[100:103], v[72:75]
	v_exp_f32_e32 v66, v66
	ds_read_b128 v[176:179], v201 offset:12288
	s_waitcnt lgkmcnt(6)
	v_mfma_f32_16x16x32_bf16 v[72:75], v[230:233], v[104:107], v[72:75]
	v_exp_f32_e32 v70, v70
	v_exp_f32_e32 v67, v67
	v_mfma_f32_16x16x32_bf16 v[76:79], v[230:233], v[120:123], v[76:79]
	v_exp_f32_e32 v71, v71
	v_add_f32_e32 v220, v64, v65
	ds_read_b128 v[180:183], v202 offset:12288
	s_waitcnt lgkmcnt(6)
	v_mfma_f32_16x16x32_bf16 v[76:79], v[234:237], v[124:127], v[76:79]
	v_add_f32_e32 v221, v68, v69
	v_add_f32_e32 v220, v220, v66
	v_add_f32_e32 v221, v221, v70
	v_mfma_f32_16x16x32_bf16 v[72:75], v[234:237], v[108:111], v[72:75]
	v_add_f32_e32 v220, v220, v67
	v_add_f32_e32 v221, v221, v71
	ds_read_b128 v[230:233], v203 offset:12288
	s_waitcnt lgkmcnt(6)
	v_mfma_f32_16x16x32_bf16 v[80:83], v[160:163], v[96:99], 0
	s_nop 7
	s_nop 1
	v_exp_f32_e32 v72, v72
	v_exp_f32_e32 v76, v76
	v_mfma_f32_16x16x32_bf16 v[84:87], v[160:163], v[112:115], 0
	v_exp_f32_e32 v73, v73
	v_exp_f32_e32 v77, v77
	ds_read_b128 v[234:237], v246 offset:12288
	s_waitcnt lgkmcnt(6)
	v_mfma_f32_16x16x32_bf16 v[84:87], v[164:167], v[116:119], v[84:87]
	v_exp_f32_e32 v74, v74
	v_exp_f32_e32 v78, v78
	v_mfma_f32_16x16x32_bf16 v[80:83], v[164:167], v[100:103], v[80:83]
	v_exp_f32_e32 v75, v75
	v_exp_f32_e32 v79, v79
	s_waitcnt lgkmcnt(5)
	v_mfma_f32_16x16x32_bf16 v[80:83], v[168:171], v[104:107], v[80:83]
	v_add_f32_e32 v220, v220, v72
	v_add_f32_e32 v221, v221, v76
	v_add_f32_e32 v220, v220, v73
	v_add_f32_e32 v221, v221, v77
	v_mfma_f32_16x16x32_bf16 v[84:87], v[168:171], v[120:123], v[84:87]
	v_add_f32_e32 v220, v220, v74
	v_add_f32_e32 v221, v221, v78
	v_add_f32_e32 v220, v220, v75
	v_add_f32_e32 v221, v221, v79
	s_waitcnt lgkmcnt(4)
	v_mfma_f32_16x16x32_bf16 v[84:87], v[172:175], v[124:127], v[84:87]
	v_cvt_pk_bf16_f32 v216, v64, v65
	v_cvt_pk_bf16_f32 v217, v66, v67
	v_cvt_pk_bf16_f32 v238, v68, v69
	v_cvt_pk_bf16_f32 v239, v70, v71
	v_mfma_f32_16x16x32_bf16 v[80:83], v[172:175], v[108:111], v[80:83]
	v_cvt_pk_bf16_f32 v218, v72, v73
	v_cvt_pk_bf16_f32 v219, v74, v75
	v_cvt_pk_bf16_f32 v240, v76, v77
	v_cvt_pk_bf16_f32 v241, v78, v79
	s_waitcnt lgkmcnt(3)
	v_mfma_f32_16x16x32_bf16 v[88:91], v[176:179], v[96:99], 0
	s_nop 7
	s_nop 1
	v_exp_f32_e32 v80, v80
	v_exp_f32_e32 v84, v84
	v_mfma_f32_16x16x32_bf16 v[92:95], v[176:179], v[112:115], 0
	v_exp_f32_e32 v81, v81
	s_waitcnt lgkmcnt(2)
	v_mfma_f32_16x16x32_bf16 v[92:95], v[180:183], v[116:119], v[92:95]
	v_exp_f32_e32 v85, v85
	v_exp_f32_e32 v82, v82
	v_mfma_f32_16x16x32_bf16 v[88:91], v[180:183], v[100:103], v[88:91]
	v_exp_f32_e32 v86, v86
	s_waitcnt lgkmcnt(1)
	v_mfma_f32_16x16x32_bf16 v[88:91], v[230:233], v[104:107], v[88:91]
	v_exp_f32_e32 v83, v83
	v_exp_f32_e32 v87, v87
	v_mfma_f32_16x16x32_bf16 v[92:95], v[230:233], v[120:123], v[92:95]
	v_add_f32_e32 v220, v220, v80
	v_add_f32_e32 v221, v221, v84
	v_add_f32_e32 v220, v220, v81
	s_waitcnt lgkmcnt(0)
	v_mfma_f32_16x16x32_bf16 v[92:95], v[234:237], v[124:127], v[92:95]
	v_add_f32_e32 v221, v221, v85
	v_add_f32_e32 v220, v220, v82
	v_add_f32_e32 v221, v221, v86
	v_mfma_f32_16x16x32_bf16 v[88:91], v[234:237], v[108:111], v[88:91]
	v_add_f32_e32 v220, v220, v83
	v_add_f32_e32 v221, v221, v87
	s_waitcnt lgkmcnt(0)
	s_barrier
	ds_read_b128 v[160:163], v201 offset:16384
	ds_read_b128 v[164:167], v209 offset:0
	ds_read_b128 v[168:171], v202 offset:16384
	ds_read_b128 v[172:175], v209 offset:2048
	ds_read_b128 v[176:179], v203 offset:16384
	ds_read_b128 v[180:183], v209 offset:4096
	ds_read_b128 v[230:233], v246 offset:16384
	ds_read_b128 v[234:237], v209 offset:6144

.Lattn_pb0:
	s_waitcnt lgkmcnt(7)
	v_mfma_f32_16x16x32_bf16 v[64:67], v[160:163], v[96:99], 0
	v_exp_f32_e32 v88, v88
	v_mfma_f32_16x16x32_bf16 v[68:71], v[160:163], v[112:115], 0
	v_exp_f32_e32 v92, v92
	ds_read_b128 v[160:163], v201 offset:20480
	s_add_u32 s16, s22, s10
	s_addc_u32 s17, s23, s11
	s_add_u32 s15, s22, s12
	s_addc_u32 s14, s23, s13
	s_add_u32 s8, s16, 0x3bc00200
	s_addc_u32 s9, s17, 0
	s_add_u32 s6, s15, 0x23a50000
	s_addc_u32 s7, s14, 0
	s_waitcnt lgkmcnt(7)
	v_mfma_f32_16x16x32_bf16 v[0:3], v[164:167], v[216:219], v[0:3]
	v_cvt_pk_bf16_f32 v242, v80, v81
	v_mfma_f32_16x16x32_bf16 v[4:7], v[164:167], v[238:241], v[4:7]
	v_exp_f32_e32 v89, v89
	ds_read_b128 v[164:167], v209 offset:8192
	s_waitcnt vmcnt(4)
	ds_write_b128 v225, v[152:155] offset:49152
	s_waitcnt lgkmcnt(8)
	v_mfma_f32_16x16x32_bf16 v[68:71], v[168:171], v[116:119], v[68:71]
	v_exp_f32_e32 v93, v93
	v_mfma_f32_16x16x32_bf16 v[64:67], v[168:171], v[100:103], v[64:67]
	v_cvt_pk_bf16_f32 v243, v82, v83
	ds_read_b128 v[168:171], v202 offset:20480
	ds_write_b128 v226, v[156:159] offset:49152
	s_waitcnt lgkmcnt(9)
	v_mfma_f32_16x16x32_bf16 v[12:15], v[172:175], v[238:241], v[12:15]
	v_exp_f32_e32 v90, v90
	v_mfma_f32_16x16x32_bf16 v[8:11], v[172:175], v[216:219], v[8:11]
	v_exp_f32_e32 v94, v94
	ds_read_b128 v[172:175], v209 offset:10240
	ds_write_b64 v227, v[132:133] offset:32768
	s_waitcnt lgkmcnt(10)
	v_mfma_f32_16x16x32_bf16 v[64:67], v[176:179], v[104:107], v[64:67]
	v_cvt_pk_bf16_f32 v204, v84, v85
	v_mfma_f32_16x16x32_bf16 v[68:71], v[176:179], v[120:123], v[68:71]
	v_exp_f32_e32 v91, v91
	ds_read_b128 v[176:179], v203 offset:20480
	ds_write_b64 v228, v[134:135] offset:32768
	s_waitcnt lgkmcnt(11)
	v_mfma_f32_16x16x32_bf16 v[16:19], v[180:183], v[216:219], v[16:19]
	v_exp_f32_e32 v95, v95
	v_mfma_f32_16x16x32_bf16 v[20:23], v[180:183], v[238:241], v[20:23]
	v_cvt_pk_bf16_f32 v205, v86, v87
	v_add_f32_e32 v220, v220, v88
	ds_read_b128 v[180:183], v209 offset:12288
	ds_write_b64 v229, v[128:129] offset:32768
	s_waitcnt lgkmcnt(12)
	v_mfma_f32_16x16x32_bf16 v[68:71], v[230:233], v[124:127], v[68:71]
	v_add_f32_e32 v221, v221, v92
	v_add_f32_e32 v220, v220, v89
	v_mfma_f32_16x16x32_bf16 v[64:67], v[230:233], v[108:111], v[64:67]
	v_add_f32_e32 v221, v221, v93
	v_cvt_pk_bf16_f32 v244, v88, v89
	ds_read_b128 v[230:233], v246 offset:20480
	ds_write_b64 v184, v[130:131] offset:32768
	s_waitcnt lgkmcnt(13)
	v_mfma_f32_16x16x32_bf16 v[28:31], v[234:237], v[238:241], v[28:31]
	v_cvt_pk_bf16_f32 v245, v90, v91
	v_cvt_pk_bf16_f32 v206, v92, v93
	v_mfma_f32_16x16x32_bf16 v[24:27], v[234:237], v[216:219], v[24:27]
	v_cvt_pk_bf16_f32 v207, v94, v95
	ds_read_b128 v[234:237], v209 offset:14336
	global_load_dwordx4 v[132:135], v198, s[8:9]
	s_waitcnt lgkmcnt(13)
	v_mfma_f32_16x16x32_bf16 v[72:75], v[160:163], v[96:99], 0
	v_add_f32_e32 v220, v220, v90
	v_add_f32_e32 v221, v221, v94
	v_mfma_f32_16x16x32_bf16 v[76:79], v[160:163], v[112:115], 0
	v_add_f32_e32 v220, v220, v91
	v_add_f32_e32 v221, v221, v95
	ds_read_b128 v[160:163], v201 offset:24576
	global_load_dwordx4 v[128:131], v199, s[8:9]
	s_waitcnt lgkmcnt(13)
	v_mfma_f32_16x16x32_bf16 v[32:35], v[164:167], v[216:219], v[32:35]
	v_add_f32_e32 v194, v194, v220
	v_add_f32_e32 v195, v195, v221
	v_mfma_f32_16x16x32_bf16 v[36:39], v[164:167], v[238:241], v[36:39]
	v_exp_f32_e32 v64, v64
	ds_read_b128 v[164:167], v210 offset:0
	global_load_dwordx4 v[152:155], v196, s[6:7]
	s_waitcnt lgkmcnt(12)
	v_mfma_f32_16x16x32_bf16 v[76:79], v[168:171], v[116:119], v[76:79]
	v_exp_f32_e32 v68, v68
	v_mfma_f32_16x16x32_bf16 v[72:75], v[168:171], v[100:103], v[72:75]
	v_exp_f32_e32 v65, v65
	ds_read_b128 v[168:171], v202 offset:24576
	global_load_dwordx4 v[156:159], v197, s[6:7]
	s_waitcnt lgkmcnt(11)
	v_mfma_f32_16x16x32_bf16 v[44:47], v[172:175], v[238:241], v[44:47]
	v_exp_f32_e32 v69, v69
	v_mfma_f32_16x16x32_bf16 v[40:43], v[172:175], v[216:219], v[40:43]
	v_exp_f32_e32 v66, v66
	ds_read_b128 v[172:175], v210 offset:2048
	s_waitcnt lgkmcnt(10)
	v_mfma_f32_16x16x32_bf16 v[72:75], v[176:179], v[104:107], v[72:75]
	v_exp_f32_e32 v70, v70
	v_mfma_f32_16x16x32_bf16 v[76:79], v[176:179], v[120:123], v[76:79]
	v_exp_f32_e32 v67, v67
	ds_read_b128 v[176:179], v203 offset:24576
	s_waitcnt lgkmcnt(9)
	v_mfma_f32_16x16x32_bf16 v[48:51], v[180:183], v[216:219], v[48:51]
	v_exp_f32_e32 v71, v71
	v_mfma_f32_16x16x32_bf16 v[52:55], v[180:183], v[238:241], v[52:55]
	v_add_f32_e32 v220, v64, v65
	ds_read_b128 v[180:183], v210 offset:4096
	s_waitcnt lgkmcnt(8)
	v_mfma_f32_16x16x32_bf16 v[76:79], v[230:233], v[124:127], v[76:79]
	v_add_f32_e32 v221, v68, v69
	v_mfma_f32_16x16x32_bf16 v[72:75], v[230:233], v[108:111], v[72:75]
	v_add_f32_e32 v220, v220, v66
	ds_read_b128 v[230:233], v246 offset:24576
	s_waitcnt lgkmcnt(7)
	v_mfma_f32_16x16x32_bf16 v[60:63], v[234:237], v[238:241], v[60:63]
	v_add_f32_e32 v221, v221, v70
	v_add_f32_e32 v220, v220, v67
	v_mfma_f32_16x16x32_bf16 v[56:59], v[234:237], v[216:219], v[56:59]
	v_add_f32_e32 v221, v221, v71
	ds_read_b128 v[234:237], v210 offset:6144
	s_waitcnt lgkmcnt(7)
	v_mfma_f32_16x16x32_bf16 v[80:83], v[160:163], v[96:99], 0
	v_exp_f32_e32 v72, v72
	v_mfma_f32_16x16x32_bf16 v[84:87], v[160:163], v[112:115], 0
	v_exp_f32_e32 v76, v76
	ds_read_b128 v[160:163], v201 offset:28672
	s_waitcnt lgkmcnt(7)
	v_mfma_f32_16x16x32_bf16 v[0:3], v[164:167], v[242:245], v[0:3]
	v_exp_f32_e32 v73, v73
	v_mfma_f32_16x16x32_bf16 v[4:7], v[164:167], v[204:207], v[4:7]
	v_exp_f32_e32 v77, v77
	ds_read_b128 v[164:167], v210 offset:8192
	s_waitcnt lgkmcnt(7)
	v_mfma_f32_16x16x32_bf16 v[84:87], v[168:171], v[116:119], v[84:87]
	v_exp_f32_e32 v74, v74
	v_mfma_f32_16x16x32_bf16 v[80:83], v[168:171], v[100:103], v[80:83]
	v_exp_f32_e32 v78, v78
	ds_read_b128 v[168:171], v202 offset:28672
	s_waitcnt lgkmcnt(7)
	v_mfma_f32_16x16x32_bf16 v[12:15], v[172:175], v[204:207], v[12:15]
	v_exp_f32_e32 v75, v75
	v_mfma_f32_16x16x32_bf16 v[8:11], v[172:175], v[242:245], v[8:11]
	v_exp_f32_e32 v79, v79
	ds_read_b128 v[172:175], v210 offset:10240
	s_waitcnt lgkmcnt(7)
	v_mfma_f32_16x16x32_bf16 v[80:83], v[176:179], v[104:107], v[80:83]
	v_add_f32_e32 v220, v220, v72
	v_add_f32_e32 v221, v221, v76
	v_mfma_f32_16x16x32_bf16 v[84:87], v[176:179], v[120:123], v[84:87]
	v_add_f32_e32 v220, v220, v73
	ds_read_b128 v[176:179], v203 offset:28672
	s_waitcnt lgkmcnt(7)
	v_mfma_f32_16x16x32_bf16 v[16:19], v[180:183], v[242:245], v[16:19]
	v_add_f32_e32 v221, v221, v77
	v_add_f32_e32 v220, v220, v74
	v_mfma_f32_16x16x32_bf16 v[20:23], v[180:183], v[204:207], v[20:23]
	v_add_f32_e32 v221, v221, v78
	ds_read_b128 v[180:183], v210 offset:12288
	s_waitcnt lgkmcnt(7)
	v_mfma_f32_16x16x32_bf16 v[84:87], v[230:233], v[124:127], v[84:87]
	v_add_f32_e32 v220, v220, v75
	v_add_f32_e32 v221, v221, v79
	v_mfma_f32_16x16x32_bf16 v[80:83], v[230:233], v[108:111], v[80:83]
	v_cvt_pk_bf16_f32 v216, v64, v65
	ds_read_b128 v[230:233], v246 offset:28672
	s_waitcnt lgkmcnt(7)
	v_mfma_f32_16x16x32_bf16 v[28:31], v[234:237], v[204:207], v[28:31]
	v_cvt_pk_bf16_f32 v217, v66, v67
	v_cvt_pk_bf16_f32 v238, v68, v69
	v_mfma_f32_16x16x32_bf16 v[24:27], v[234:237], v[242:245], v[24:27]
	v_cvt_pk_bf16_f32 v239, v70, v71
	ds_read_b128 v[234:237], v210 offset:14336
	s_waitcnt lgkmcnt(7)
	v_mfma_f32_16x16x32_bf16 v[88:91], v[160:163], v[96:99], 0
	v_exp_f32_e32 v80, v80
	v_mfma_f32_16x16x32_bf16 v[92:95], v[160:163], v[112:115], 0
	v_exp_f32_e32 v84, v84
	ds_read_b128 v[160:163], v201 offset:32768
	s_waitcnt lgkmcnt(7)
	v_mfma_f32_16x16x32_bf16 v[32:35], v[164:167], v[242:245], v[32:35]
	v_exp_f32_e32 v81, v81
	v_mfma_f32_16x16x32_bf16 v[36:39], v[164:167], v[204:207], v[36:39]
	v_exp_f32_e32 v85, v85
	ds_read_b128 v[164:167], v209 offset:16384
	s_waitcnt lgkmcnt(7)
	v_mfma_f32_16x16x32_bf16 v[92:95], v[168:171], v[116:119], v[92:95]
	v_exp_f32_e32 v82, v82
	v_mfma_f32_16x16x32_bf16 v[88:91], v[168:171], v[100:103], v[88:91]
	v_exp_f32_e32 v86, v86
	ds_read_b128 v[168:171], v202 offset:32768
	s_waitcnt lgkmcnt(7)
	v_mfma_f32_16x16x32_bf16 v[44:47], v[172:175], v[204:207], v[44:47]
	v_exp_f32_e32 v83, v83
	v_mfma_f32_16x16x32_bf16 v[40:43], v[172:175], v[242:245], v[40:43]
	v_exp_f32_e32 v87, v87
	ds_read_b128 v[172:175], v209 offset:18432
	s_waitcnt lgkmcnt(7)
	v_mfma_f32_16x16x32_bf16 v[88:91], v[176:179], v[104:107], v[88:91]
	v_add_f32_e32 v220, v220, v80
	v_add_f32_e32 v221, v221, v84
	v_mfma_f32_16x16x32_bf16 v[92:95], v[176:179], v[120:123], v[92:95]
	v_add_f32_e32 v220, v220, v81
	ds_read_b128 v[176:179], v203 offset:32768
	s_waitcnt lgkmcnt(7)
	v_mfma_f32_16x16x32_bf16 v[48:51], v[180:183], v[242:245], v[48:51]
	v_add_f32_e32 v221, v221, v85
	v_add_f32_e32 v220, v220, v82
	v_mfma_f32_16x16x32_bf16 v[52:55], v[180:183], v[204:207], v[52:55]
	v_add_f32_e32 v221, v221, v86
	ds_read_b128 v[180:183], v209 offset:20480
	s_waitcnt lgkmcnt(7)
	v_mfma_f32_16x16x32_bf16 v[92:95], v[230:233], v[124:127], v[92:95]
	v_add_f32_e32 v220, v220, v83
	v_add_f32_e32 v221, v221, v87
	v_mfma_f32_16x16x32_bf16 v[88:91], v[230:233], v[108:111], v[88:91]
	v_cvt_pk_bf16_f32 v218, v72, v73
	ds_read_b128 v[230:233], v246 offset:32768
	s_waitcnt lgkmcnt(7)
	v_mfma_f32_16x16x32_bf16 v[60:63], v[234:237], v[204:207], v[60:63]
	v_cvt_pk_bf16_f32 v219, v74, v75
	v_cvt_pk_bf16_f32 v240, v76, v77
	v_mfma_f32_16x16x32_bf16 v[56:59], v[234:237], v[242:245], v[56:59]
	v_cvt_pk_bf16_f32 v241, v78, v79
	ds_read_b128 v[234:237], v209 offset:22528
	s_cmp_eq_u32 s100, 1
	s_cbranch_scc1 .Lattn_pa1
	s_setprio 1
	s_branch .Lattn_pb1

.Lattn_pb1:
	s_waitcnt lgkmcnt(7)
	v_mfma_f32_16x16x32_bf16 v[64:67], v[160:163], v[96:99], 0
	v_exp_f32_e32 v88, v88
	v_mfma_f32_16x16x32_bf16 v[68:71], v[160:163], v[112:115], 0
	v_exp_f32_e32 v92, v92
	ds_read_b128 v[160:163], v201 offset:36864
	s_add_u32 s8, s16, 0x3bc00280
	s_addc_u32 s9, s17, 0
	s_add_u32 s6, s15, 0x23a60000
	s_addc_u32 s7, s14, 0
	s_waitcnt lgkmcnt(7)
	v_mfma_f32_16x16x32_bf16 v[0:3], v[164:167], v[216:219], v[0:3]
	v_cvt_pk_bf16_f32 v242, v80, v81
	v_mfma_f32_16x16x32_bf16 v[4:7], v[164:167], v[238:241], v[4:7]
	v_exp_f32_e32 v89, v89
	ds_read_b128 v[164:167], v209 offset:24576
	s_waitcnt vmcnt(4)
	ds_write_b128 v225, v[136:139] offset:0
	s_waitcnt lgkmcnt(8)
	v_mfma_f32_16x16x32_bf16 v[68:71], v[168:171], v[116:119], v[68:71]
	v_exp_f32_e32 v93, v93
	v_mfma_f32_16x16x32_bf16 v[64:67], v[168:171], v[100:103], v[64:67]
	v_cvt_pk_bf16_f32 v243, v82, v83
	ds_read_b128 v[168:171], v202 offset:36864
	ds_write_b128 v226, v[140:143] offset:0
	s_waitcnt lgkmcnt(9)
	v_mfma_f32_16x16x32_bf16 v[12:15], v[172:175], v[238:241], v[12:15]
	v_exp_f32_e32 v90, v90
	v_mfma_f32_16x16x32_bf16 v[8:11], v[172:175], v[216:219], v[8:11]
	v_exp_f32_e32 v94, v94
	ds_read_b128 v[172:175], v209 offset:26624
	ds_write_b64 v227, v[148:149] offset:49152
	s_waitcnt lgkmcnt(10)
	v_mfma_f32_16x16x32_bf16 v[64:67], v[176:179], v[104:107], v[64:67]
	v_cvt_pk_bf16_f32 v204, v84, v85
	v_mfma_f32_16x16x32_bf16 v[68:71], v[176:179], v[120:123], v[68:71]
	v_exp_f32_e32 v91, v91
	ds_read_b128 v[176:179], v203 offset:36864
	ds_write_b64 v228, v[150:151] offset:49152
	s_waitcnt lgkmcnt(11)
	v_mfma_f32_16x16x32_bf16 v[16:19], v[180:183], v[216:219], v[16:19]
	v_exp_f32_e32 v95, v95
	v_mfma_f32_16x16x32_bf16 v[20:23], v[180:183], v[238:241], v[20:23]
	v_cvt_pk_bf16_f32 v205, v86, v87
	v_add_f32_e32 v220, v220, v88
	ds_read_b128 v[180:183], v209 offset:28672
	ds_write_b64 v229, v[144:145] offset:49152
	s_waitcnt lgkmcnt(12)
	v_mfma_f32_16x16x32_bf16 v[68:71], v[230:233], v[124:127], v[68:71]
	v_add_f32_e32 v221, v221, v92
	v_add_f32_e32 v220, v220, v89
	v_mfma_f32_16x16x32_bf16 v[64:67], v[230:233], v[108:111], v[64:67]
	v_add_f32_e32 v221, v221, v93
	v_cvt_pk_bf16_f32 v244, v88, v89
	ds_read_b128 v[230:233], v246 offset:36864
	ds_write_b64 v184, v[146:147] offset:49152
	s_waitcnt lgkmcnt(13)
	v_mfma_f32_16x16x32_bf16 v[28:31], v[234:237], v[238:241], v[28:31]
	v_cvt_pk_bf16_f32 v245, v90, v91
	v_cvt_pk_bf16_f32 v206, v92, v93
	v_mfma_f32_16x16x32_bf16 v[24:27], v[234:237], v[216:219], v[24:27]
	v_cvt_pk_bf16_f32 v207, v94, v95
	ds_read_b128 v[234:237], v209 offset:30720
	global_load_dwordx4 v[148:151], v198, s[8:9]
	s_waitcnt lgkmcnt(13)
	v_mfma_f32_16x16x32_bf16 v[72:75], v[160:163], v[96:99], 0
	v_add_f32_e32 v220, v220, v90
	v_add_f32_e32 v221, v221, v94
	v_mfma_f32_16x16x32_bf16 v[76:79], v[160:163], v[112:115], 0
	v_add_f32_e32 v220, v220, v91
	v_add_f32_e32 v221, v221, v95
	ds_read_b128 v[160:163], v201 offset:40960
	global_load_dwordx4 v[144:147], v199, s[8:9]
	s_waitcnt lgkmcnt(13)
	v_mfma_f32_16x16x32_bf16 v[32:35], v[164:167], v[216:219], v[32:35]
	v_add_f32_e32 v194, v194, v220
	v_add_f32_e32 v195, v195, v221
	v_mfma_f32_16x16x32_bf16 v[36:39], v[164:167], v[238:241], v[36:39]
	v_exp_f32_e32 v64, v64
	ds_read_b128 v[164:167], v210 offset:16384
	global_load_dwordx4 v[136:139], v196, s[6:7]
	s_waitcnt lgkmcnt(12)
	v_mfma_f32_16x16x32_bf16 v[76:79], v[168:171], v[116:119], v[76:79]
	v_exp_f32_e32 v68, v68
	v_mfma_f32_16x16x32_bf16 v[72:75], v[168:171], v[100:103], v[72:75]
	v_exp_f32_e32 v65, v65
	ds_read_b128 v[168:171], v202 offset:40960
	global_load_dwordx4 v[140:143], v197, s[6:7]
	s_waitcnt lgkmcnt(11)
	v_mfma_f32_16x16x32_bf16 v[44:47], v[172:175], v[238:241], v[44:47]
	v_exp_f32_e32 v69, v69
	v_mfma_f32_16x16x32_bf16 v[40:43], v[172:175], v[216:219], v[40:43]
	v_exp_f32_e32 v66, v66
	ds_read_b128 v[172:175], v210 offset:18432
	s_waitcnt lgkmcnt(10)
	v_mfma_f32_16x16x32_bf16 v[72:75], v[176:179], v[104:107], v[72:75]
	v_exp_f32_e32 v70, v70
	v_mfma_f32_16x16x32_bf16 v[76:79], v[176:179], v[120:123], v[76:79]
	v_exp_f32_e32 v67, v67
	ds_read_b128 v[176:179], v203 offset:40960
	s_waitcnt lgkmcnt(9)
	v_mfma_f32_16x16x32_bf16 v[48:51], v[180:183], v[216:219], v[48:51]
	v_exp_f32_e32 v71, v71
	v_mfma_f32_16x16x32_bf16 v[52:55], v[180:183], v[238:241], v[52:55]
	v_add_f32_e32 v220, v64, v65
	ds_read_b128 v[180:183], v210 offset:20480
	s_waitcnt lgkmcnt(8)
	v_mfma_f32_16x16x32_bf16 v[76:79], v[230:233], v[124:127], v[76:79]
	v_add_f32_e32 v221, v68, v69
	v_mfma_f32_16x16x32_bf16 v[72:75], v[230:233], v[108:111], v[72:75]
	v_add_f32_e32 v220, v220, v66
	ds_read_b128 v[230:233], v246 offset:40960
	s_waitcnt lgkmcnt(7)
	v_mfma_f32_16x16x32_bf16 v[60:63], v[234:237], v[238:241], v[60:63]
	v_add_f32_e32 v221, v221, v70
	v_add_f32_e32 v220, v220, v67
	v_mfma_f32_16x16x32_bf16 v[56:59], v[234:237], v[216:219], v[56:59]
	v_add_f32_e32 v221, v221, v71
	ds_read_b128 v[234:237], v210 offset:22528
	s_waitcnt lgkmcnt(7)
	v_mfma_f32_16x16x32_bf16 v[80:83], v[160:163], v[96:99], 0
	v_exp_f32_e32 v72, v72
	v_mfma_f32_16x16x32_bf16 v[84:87], v[160:163], v[112:115], 0
	v_exp_f32_e32 v76, v76
	ds_read_b128 v[160:163], v201 offset:45056
	s_waitcnt lgkmcnt(7)
	v_mfma_f32_16x16x32_bf16 v[0:3], v[164:167], v[242:245], v[0:3]
	v_exp_f32_e32 v73, v73
	v_mfma_f32_16x16x32_bf16 v[4:7], v[164:167], v[204:207], v[4:7]
	v_exp_f32_e32 v77, v77
	ds_read_b128 v[164:167], v210 offset:24576
	s_waitcnt lgkmcnt(7)
	v_mfma_f32_16x16x32_bf16 v[84:87], v[168:171], v[116:119], v[84:87]
	v_exp_f32_e32 v74, v74
	v_mfma_f32_16x16x32_bf16 v[80:83], v[168:171], v[100:103], v[80:83]
	v_exp_f32_e32 v78, v78
	ds_read_b128 v[168:171], v202 offset:45056
	s_waitcnt lgkmcnt(7)
	v_mfma_f32_16x16x32_bf16 v[12:15], v[172:175], v[204:207], v[12:15]
	v_exp_f32_e32 v75, v75
	v_mfma_f32_16x16x32_bf16 v[8:11], v[172:175], v[242:245], v[8:11]
	v_exp_f32_e32 v79, v79
	ds_read_b128 v[172:175], v210 offset:26624
	s_waitcnt lgkmcnt(7)
	v_mfma_f32_16x16x32_bf16 v[80:83], v[176:179], v[104:107], v[80:83]
	v_add_f32_e32 v220, v220, v72
	v_add_f32_e32 v221, v221, v76
	v_mfma_f32_16x16x32_bf16 v[84:87], v[176:179], v[120:123], v[84:87]
	v_add_f32_e32 v220, v220, v73
	ds_read_b128 v[176:179], v203 offset:45056
	s_waitcnt lgkmcnt(7)
	v_mfma_f32_16x16x32_bf16 v[16:19], v[180:183], v[242:245], v[16:19]
	v_add_f32_e32 v221, v221, v77
	v_add_f32_e32 v220, v220, v74
	v_mfma_f32_16x16x32_bf16 v[20:23], v[180:183], v[204:207], v[20:23]
	v_add_f32_e32 v221, v221, v78
	ds_read_b128 v[180:183], v210 offset:28672
	s_waitcnt lgkmcnt(7)
	v_mfma_f32_16x16x32_bf16 v[84:87], v[230:233], v[124:127], v[84:87]
	v_add_f32_e32 v220, v220, v75
	v_add_f32_e32 v221, v221, v79
	v_mfma_f32_16x16x32_bf16 v[80:83], v[230:233], v[108:111], v[80:83]
	v_cvt_pk_bf16_f32 v216, v64, v65
	ds_read_b128 v[230:233], v246 offset:45056
	s_waitcnt lgkmcnt(7)
	v_mfma_f32_16x16x32_bf16 v[28:31], v[234:237], v[204:207], v[28:31]
	v_cvt_pk_bf16_f32 v217, v66, v67
	v_cvt_pk_bf16_f32 v238, v68, v69
	v_mfma_f32_16x16x32_bf16 v[24:27], v[234:237], v[242:245], v[24:27]
	v_cvt_pk_bf16_f32 v239, v70, v71
	ds_read_b128 v[234:237], v210 offset:30720
	s_waitcnt lgkmcnt(7)
	v_mfma_f32_16x16x32_bf16 v[88:91], v[160:163], v[96:99], 0
	v_exp_f32_e32 v80, v80
	v_mfma_f32_16x16x32_bf16 v[92:95], v[160:163], v[112:115], 0
	v_exp_f32_e32 v84, v84
	s_waitcnt lgkmcnt(6)
	v_mfma_f32_16x16x32_bf16 v[32:35], v[164:167], v[242:245], v[32:35]
	v_exp_f32_e32 v81, v81
	v_mfma_f32_16x16x32_bf16 v[36:39], v[164:167], v[204:207], v[36:39]
	v_exp_f32_e32 v85, v85
	s_waitcnt lgkmcnt(5)
	v_mfma_f32_16x16x32_bf16 v[92:95], v[168:171], v[116:119], v[92:95]
	v_exp_f32_e32 v82, v82
	v_mfma_f32_16x16x32_bf16 v[88:91], v[168:171], v[100:103], v[88:91]
	v_exp_f32_e32 v86, v86
	s_waitcnt lgkmcnt(4)
	v_mfma_f32_16x16x32_bf16 v[44:47], v[172:175], v[204:207], v[44:47]
	v_exp_f32_e32 v83, v83
	v_mfma_f32_16x16x32_bf16 v[40:43], v[172:175], v[242:245], v[40:43]
	v_exp_f32_e32 v87, v87
	s_waitcnt lgkmcnt(3)
	v_mfma_f32_16x16x32_bf16 v[88:91], v[176:179], v[104:107], v[88:91]
	v_add_f32_e32 v220, v220, v80
	v_add_f32_e32 v221, v221, v84
	v_mfma_f32_16x16x32_bf16 v[92:95], v[176:179], v[120:123], v[92:95]
	v_add_f32_e32 v220, v220, v81
	s_waitcnt lgkmcnt(0)
	s_barrier
	ds_read_b128 v[160:163], v201 offset:49152
	ds_read_b128 v[164:167], v209 offset:32768
	ds_read_b128 v[168:171], v202 offset:49152
	ds_read_b128 v[172:175], v209 offset:34816
	ds_read_b128 v[176:179], v203 offset:49152
	v_mfma_f32_16x16x32_bf16 v[48:51], v[180:183], v[242:245], v[48:51]
	v_add_f32_e32 v221, v221, v85
	v_add_f32_e32 v220, v220, v82
	v_mfma_f32_16x16x32_bf16 v[52:55], v[180:183], v[204:207], v[52:55]
	v_add_f32_e32 v221, v221, v86
	ds_read_b128 v[180:183], v209 offset:36864
	v_mfma_f32_16x16x32_bf16 v[92:95], v[230:233], v[124:127], v[92:95]
	v_add_f32_e32 v220, v220, v83
	v_add_f32_e32 v221, v221, v87
	v_mfma_f32_16x16x32_bf16 v[88:91], v[230:233], v[108:111], v[88:91]
	v_cvt_pk_bf16_f32 v218, v72, v73
	ds_read_b128 v[230:233], v246 offset:49152
	v_mfma_f32_16x16x32_bf16 v[60:63], v[234:237], v[204:207], v[60:63]
	v_cvt_pk_bf16_f32 v219, v74, v75
	v_cvt_pk_bf16_f32 v240, v76, v77
	v_mfma_f32_16x16x32_bf16 v[56:59], v[234:237], v[242:245], v[56:59]
	v_cvt_pk_bf16_f32 v241, v78, v79
	ds_read_b128 v[234:237], v209 offset:38912
	s_cmp_eq_u32 s100, 0
	s_cbranch_scc1 .Lattn_pa2
	s_setprio 1
	s_branch .Lattn_pb2

.Lattn_pb2:
	s_waitcnt lgkmcnt(7)
	v_mfma_f32_16x16x32_bf16 v[64:67], v[160:163], v[96:99], 0
	v_exp_f32_e32 v88, v88
	v_mfma_f32_16x16x32_bf16 v[68:71], v[160:163], v[112:115], 0
	v_exp_f32_e32 v92, v92
	ds_read_b128 v[160:163], v201 offset:53248
	s_add_u32 s8, s16, 0x3bc00300
	s_addc_u32 s9, s17, 0
	s_add_u32 s6, s15, 0x23a70000
	s_addc_u32 s7, s14, 0
	s_waitcnt lgkmcnt(7)
	v_mfma_f32_16x16x32_bf16 v[0:3], v[164:167], v[216:219], v[0:3]
	v_cvt_pk_bf16_f32 v242, v80, v81
	v_mfma_f32_16x16x32_bf16 v[4:7], v[164:167], v[238:241], v[4:7]
	v_exp_f32_e32 v89, v89
	ds_read_b128 v[164:167], v209 offset:40960
	s_waitcnt vmcnt(4)
	ds_write_b128 v225, v[152:155] offset:16384
	s_waitcnt lgkmcnt(8)
	v_mfma_f32_16x16x32_bf16 v[68:71], v[168:171], v[116:119], v[68:71]
	v_exp_f32_e32 v93, v93
	v_mfma_f32_16x16x32_bf16 v[64:67], v[168:171], v[100:103], v[64:67]
	v_cvt_pk_bf16_f32 v243, v82, v83
	ds_read_b128 v[168:171], v202 offset:53248
	ds_write_b128 v226, v[156:159] offset:16384
	s_waitcnt lgkmcnt(9)
	v_mfma_f32_16x16x32_bf16 v[12:15], v[172:175], v[238:241], v[12:15]
	v_exp_f32_e32 v90, v90
	v_mfma_f32_16x16x32_bf16 v[8:11], v[172:175], v[216:219], v[8:11]
	v_exp_f32_e32 v94, v94
	ds_read_b128 v[172:175], v209 offset:43008
	ds_write_b64 v227, v[132:133] offset:0
	s_waitcnt lgkmcnt(10)
	v_mfma_f32_16x16x32_bf16 v[64:67], v[176:179], v[104:107], v[64:67]
	v_cvt_pk_bf16_f32 v204, v84, v85
	v_mfma_f32_16x16x32_bf16 v[68:71], v[176:179], v[120:123], v[68:71]
	v_exp_f32_e32 v91, v91
	ds_read_b128 v[176:179], v203 offset:53248
	ds_write_b64 v228, v[134:135] offset:0
	s_waitcnt lgkmcnt(11)
	v_mfma_f32_16x16x32_bf16 v[16:19], v[180:183], v[216:219], v[16:19]
	v_exp_f32_e32 v95, v95
	v_mfma_f32_16x16x32_bf16 v[20:23], v[180:183], v[238:241], v[20:23]
	v_cvt_pk_bf16_f32 v205, v86, v87
	v_add_f32_e32 v220, v220, v88
	ds_read_b128 v[180:183], v209 offset:45056
	ds_write_b64 v229, v[128:129] offset:0
	s_waitcnt lgkmcnt(12)
	v_mfma_f32_16x16x32_bf16 v[68:71], v[230:233], v[124:127], v[68:71]
	v_add_f32_e32 v221, v221, v92
	v_add_f32_e32 v220, v220, v89
	v_mfma_f32_16x16x32_bf16 v[64:67], v[230:233], v[108:111], v[64:67]
	v_add_f32_e32 v221, v221, v93
	v_cvt_pk_bf16_f32 v244, v88, v89
	ds_read_b128 v[230:233], v246 offset:53248
	ds_write_b64 v184, v[130:131] offset:0
	s_waitcnt lgkmcnt(13)
	v_mfma_f32_16x16x32_bf16 v[28:31], v[234:237], v[238:241], v[28:31]
	v_cvt_pk_bf16_f32 v245, v90, v91
	v_cvt_pk_bf16_f32 v206, v92, v93
	v_mfma_f32_16x16x32_bf16 v[24:27], v[234:237], v[216:219], v[24:27]
	v_cvt_pk_bf16_f32 v207, v94, v95
	ds_read_b128 v[234:237], v209 offset:47104
	global_load_dwordx4 v[132:135], v198, s[8:9]
	s_waitcnt lgkmcnt(13)
	v_mfma_f32_16x16x32_bf16 v[72:75], v[160:163], v[96:99], 0
	v_add_f32_e32 v220, v220, v90
	v_add_f32_e32 v221, v221, v94
	v_mfma_f32_16x16x32_bf16 v[76:79], v[160:163], v[112:115], 0
	v_add_f32_e32 v220, v220, v91
	v_add_f32_e32 v221, v221, v95
	ds_read_b128 v[160:163], v201 offset:57344
	global_load_dwordx4 v[128:131], v199, s[8:9]
	s_waitcnt lgkmcnt(13)
	v_mfma_f32_16x16x32_bf16 v[32:35], v[164:167], v[216:219], v[32:35]
	v_add_f32_e32 v194, v194, v220
	v_add_f32_e32 v195, v195, v221
	v_mfma_f32_16x16x32_bf16 v[36:39], v[164:167], v[238:241], v[36:39]
	v_exp_f32_e32 v64, v64
	ds_read_b128 v[164:167], v210 offset:32768
	global_load_dwordx4 v[152:155], v196, s[6:7]
	s_waitcnt lgkmcnt(12)
	v_mfma_f32_16x16x32_bf16 v[76:79], v[168:171], v[116:119], v[76:79]
	v_exp_f32_e32 v68, v68
	v_mfma_f32_16x16x32_bf16 v[72:75], v[168:171], v[100:103], v[72:75]
	v_exp_f32_e32 v65, v65
	ds_read_b128 v[168:171], v202 offset:57344
	global_load_dwordx4 v[156:159], v197, s[6:7]
	s_waitcnt lgkmcnt(11)
	v_mfma_f32_16x16x32_bf16 v[44:47], v[172:175], v[238:241], v[44:47]
	v_exp_f32_e32 v69, v69
	v_mfma_f32_16x16x32_bf16 v[40:43], v[172:175], v[216:219], v[40:43]
	v_exp_f32_e32 v66, v66
	ds_read_b128 v[172:175], v210 offset:34816
	s_waitcnt lgkmcnt(10)
	v_mfma_f32_16x16x32_bf16 v[72:75], v[176:179], v[104:107], v[72:75]
	v_exp_f32_e32 v70, v70
	v_mfma_f32_16x16x32_bf16 v[76:79], v[176:179], v[120:123], v[76:79]
	v_exp_f32_e32 v67, v67
	ds_read_b128 v[176:179], v203 offset:57344
	s_waitcnt lgkmcnt(9)
	v_mfma_f32_16x16x32_bf16 v[48:51], v[180:183], v[216:219], v[48:51]
	v_exp_f32_e32 v71, v71
	v_mfma_f32_16x16x32_bf16 v[52:55], v[180:183], v[238:241], v[52:55]
	v_add_f32_e32 v220, v64, v65
	ds_read_b128 v[180:183], v210 offset:36864
	s_waitcnt lgkmcnt(8)
	v_mfma_f32_16x16x32_bf16 v[76:79], v[230:233], v[124:127], v[76:79]
	v_add_f32_e32 v221, v68, v69
	v_mfma_f32_16x16x32_bf16 v[72:75], v[230:233], v[108:111], v[72:75]
	v_add_f32_e32 v220, v220, v66
	ds_read_b128 v[230:233], v246 offset:57344
	s_waitcnt lgkmcnt(7)
	v_mfma_f32_16x16x32_bf16 v[60:63], v[234:237], v[238:241], v[60:63]
	v_add_f32_e32 v221, v221, v70
	v_add_f32_e32 v220, v220, v67
	v_mfma_f32_16x16x32_bf16 v[56:59], v[234:237], v[216:219], v[56:59]
	v_add_f32_e32 v221, v221, v71
	ds_read_b128 v[234:237], v210 offset:38912
	s_waitcnt lgkmcnt(7)
	v_mfma_f32_16x16x32_bf16 v[80:83], v[160:163], v[96:99], 0
	v_exp_f32_e32 v72, v72
	v_mfma_f32_16x16x32_bf16 v[84:87], v[160:163], v[112:115], 0
	v_exp_f32_e32 v76, v76
	ds_read_b128 v[160:163], v201 offset:61440
	s_waitcnt lgkmcnt(7)
	v_mfma_f32_16x16x32_bf16 v[0:3], v[164:167], v[242:245], v[0:3]
	v_exp_f32_e32 v73, v73
	v_mfma_f32_16x16x32_bf16 v[4:7], v[164:167], v[204:207], v[4:7]
	v_exp_f32_e32 v77, v77
	ds_read_b128 v[164:167], v210 offset:40960
	s_waitcnt lgkmcnt(7)
	v_mfma_f32_16x16x32_bf16 v[84:87], v[168:171], v[116:119], v[84:87]
	v_exp_f32_e32 v74, v74
	v_mfma_f32_16x16x32_bf16 v[80:83], v[168:171], v[100:103], v[80:83]
	v_exp_f32_e32 v78, v78
	ds_read_b128 v[168:171], v202 offset:61440
	s_waitcnt lgkmcnt(7)
	v_mfma_f32_16x16x32_bf16 v[12:15], v[172:175], v[204:207], v[12:15]
	v_exp_f32_e32 v75, v75
	v_mfma_f32_16x16x32_bf16 v[8:11], v[172:175], v[242:245], v[8:11]
	v_exp_f32_e32 v79, v79
	ds_read_b128 v[172:175], v210 offset:43008
	s_waitcnt lgkmcnt(7)
	v_mfma_f32_16x16x32_bf16 v[80:83], v[176:179], v[104:107], v[80:83]
	v_add_f32_e32 v220, v220, v72
	v_add_f32_e32 v221, v221, v76
	v_mfma_f32_16x16x32_bf16 v[84:87], v[176:179], v[120:123], v[84:87]
	v_add_f32_e32 v220, v220, v73
	ds_read_b128 v[176:179], v203 offset:61440
	s_waitcnt lgkmcnt(7)
	v_mfma_f32_16x16x32_bf16 v[16:19], v[180:183], v[242:245], v[16:19]
	v_add_f32_e32 v221, v221, v77
	v_add_f32_e32 v220, v220, v74
	v_mfma_f32_16x16x32_bf16 v[20:23], v[180:183], v[204:207], v[20:23]
	v_add_f32_e32 v221, v221, v78
	ds_read_b128 v[180:183], v210 offset:45056
	s_waitcnt lgkmcnt(7)
	v_mfma_f32_16x16x32_bf16 v[84:87], v[230:233], v[124:127], v[84:87]
	v_add_f32_e32 v220, v220, v75
	v_add_f32_e32 v221, v221, v79
	v_mfma_f32_16x16x32_bf16 v[80:83], v[230:233], v[108:111], v[80:83]
	v_cvt_pk_bf16_f32 v216, v64, v65
	ds_read_b128 v[230:233], v246 offset:61440
	s_waitcnt lgkmcnt(7)
	v_mfma_f32_16x16x32_bf16 v[28:31], v[234:237], v[204:207], v[28:31]
	v_cvt_pk_bf16_f32 v217, v66, v67
	v_cvt_pk_bf16_f32 v238, v68, v69
	v_mfma_f32_16x16x32_bf16 v[24:27], v[234:237], v[242:245], v[24:27]
	v_cvt_pk_bf16_f32 v239, v70, v71
	ds_read_b128 v[234:237], v210 offset:47104
	s_waitcnt lgkmcnt(7)
	v_mfma_f32_16x16x32_bf16 v[88:91], v[160:163], v[96:99], 0
	v_exp_f32_e32 v80, v80
	v_mfma_f32_16x16x32_bf16 v[92:95], v[160:163], v[112:115], 0
	v_exp_f32_e32 v84, v84
	ds_read_b128 v[160:163], v201 offset:0
	s_waitcnt lgkmcnt(7)
	v_mfma_f32_16x16x32_bf16 v[32:35], v[164:167], v[242:245], v[32:35]
	v_exp_f32_e32 v81, v81
	v_mfma_f32_16x16x32_bf16 v[36:39], v[164:167], v[204:207], v[36:39]
	v_exp_f32_e32 v85, v85
	ds_read_b128 v[164:167], v209 offset:49152
	s_waitcnt lgkmcnt(7)
	v_mfma_f32_16x16x32_bf16 v[92:95], v[168:171], v[116:119], v[92:95]
	v_exp_f32_e32 v82, v82
	v_mfma_f32_16x16x32_bf16 v[88:91], v[168:171], v[100:103], v[88:91]
	v_exp_f32_e32 v86, v86
	ds_read_b128 v[168:171], v202 offset:0
	s_waitcnt lgkmcnt(7)
	v_mfma_f32_16x16x32_bf16 v[44:47], v[172:175], v[204:207], v[44:47]
	v_exp_f32_e32 v83, v83
	v_mfma_f32_16x16x32_bf16 v[40:43], v[172:175], v[242:245], v[40:43]
	v_exp_f32_e32 v87, v87
	ds_read_b128 v[172:175], v209 offset:51200
	s_waitcnt lgkmcnt(7)
	v_mfma_f32_16x16x32_bf16 v[88:91], v[176:179], v[104:107], v[88:91]
	v_add_f32_e32 v220, v220, v80
	v_add_f32_e32 v221, v221, v84
	v_mfma_f32_16x16x32_bf16 v[92:95], v[176:179], v[120:123], v[92:95]
	v_add_f32_e32 v220, v220, v81
	ds_read_b128 v[176:179], v203 offset:0
	s_waitcnt lgkmcnt(7)
	v_mfma_f32_16x16x32_bf16 v[48:51], v[180:183], v[242:245], v[48:51]
	v_add_f32_e32 v221, v221, v85
	v_add_f32_e32 v220, v220, v82
	v_mfma_f32_16x16x32_bf16 v[52:55], v[180:183], v[204:207], v[52:55]
	v_add_f32_e32 v221, v221, v86
	ds_read_b128 v[180:183], v209 offset:53248
	s_waitcnt lgkmcnt(7)
	v_mfma_f32_16x16x32_bf16 v[92:95], v[230:233], v[124:127], v[92:95]
	v_add_f32_e32 v220, v220, v83
	v_add_f32_e32 v221, v221, v87
	v_mfma_f32_16x16x32_bf16 v[88:91], v[230:233], v[108:111], v[88:91]
	v_cvt_pk_bf16_f32 v218, v72, v73
	ds_read_b128 v[230:233], v246 offset:0
	s_waitcnt lgkmcnt(7)
	v_mfma_f32_16x16x32_bf16 v[60:63], v[234:237], v[204:207], v[60:63]
	v_cvt_pk_bf16_f32 v219, v74, v75
	v_cvt_pk_bf16_f32 v240, v76, v77
	v_mfma_f32_16x16x32_bf16 v[56:59], v[234:237], v[242:245], v[56:59]
	v_cvt_pk_bf16_f32 v241, v78, v79
	ds_read_b128 v[234:237], v209 offset:55296
	s_cmp_eq_u32 s100, 1
	s_cbranch_scc1 .Lattn_pa3
	s_setprio 1
	s_branch .Lattn_pb3

.Lattn_pb3:
	s_waitcnt lgkmcnt(7)
	v_mfma_f32_16x16x32_bf16 v[64:67], v[160:163], v[96:99], 0
	v_exp_f32_e32 v88, v88
	v_mfma_f32_16x16x32_bf16 v[68:71], v[160:163], v[112:115], 0
	v_exp_f32_e32 v92, v92
	ds_read_b128 v[160:163], v201 offset:4096
	s_add_u32 s8, s16, 0x3bc00380
	s_addc_u32 s9, s17, 0
	s_add_u32 s6, s15, 0x23a80000
	s_addc_u32 s7, s14, 0
	s_waitcnt lgkmcnt(7)
	v_mfma_f32_16x16x32_bf16 v[0:3], v[164:167], v[216:219], v[0:3]
	v_cvt_pk_bf16_f32 v242, v80, v81
	v_mfma_f32_16x16x32_bf16 v[4:7], v[164:167], v[238:241], v[4:7]
	v_exp_f32_e32 v89, v89
	ds_read_b128 v[164:167], v209 offset:57344
	s_waitcnt vmcnt(4)
	ds_write_b128 v225, v[136:139] offset:32768
	s_waitcnt lgkmcnt(8)
	v_mfma_f32_16x16x32_bf16 v[68:71], v[168:171], v[116:119], v[68:71]
	v_exp_f32_e32 v93, v93
	v_mfma_f32_16x16x32_bf16 v[64:67], v[168:171], v[100:103], v[64:67]
	v_cvt_pk_bf16_f32 v243, v82, v83
	ds_read_b128 v[168:171], v202 offset:4096
	ds_write_b128 v226, v[140:143] offset:32768
	s_waitcnt lgkmcnt(9)
	v_mfma_f32_16x16x32_bf16 v[12:15], v[172:175], v[238:241], v[12:15]
	v_exp_f32_e32 v90, v90
	v_mfma_f32_16x16x32_bf16 v[8:11], v[172:175], v[216:219], v[8:11]
	v_exp_f32_e32 v94, v94
	ds_read_b128 v[172:175], v209 offset:59392
	ds_write_b64 v227, v[148:149] offset:16384
	s_waitcnt lgkmcnt(10)
	v_mfma_f32_16x16x32_bf16 v[64:67], v[176:179], v[104:107], v[64:67]
	v_cvt_pk_bf16_f32 v204, v84, v85
	v_mfma_f32_16x16x32_bf16 v[68:71], v[176:179], v[120:123], v[68:71]
	v_exp_f32_e32 v91, v91
	ds_read_b128 v[176:179], v203 offset:4096
	ds_write_b64 v228, v[150:151] offset:16384
	s_waitcnt lgkmcnt(11)
	v_mfma_f32_16x16x32_bf16 v[16:19], v[180:183], v[216:219], v[16:19]
	v_exp_f32_e32 v95, v95
	v_mfma_f32_16x16x32_bf16 v[20:23], v[180:183], v[238:241], v[20:23]
	v_cvt_pk_bf16_f32 v205, v86, v87
	v_add_f32_e32 v220, v220, v88
	ds_read_b128 v[180:183], v209 offset:61440
	ds_write_b64 v229, v[144:145] offset:16384
	s_waitcnt lgkmcnt(12)
	v_mfma_f32_16x16x32_bf16 v[68:71], v[230:233], v[124:127], v[68:71]
	v_add_f32_e32 v221, v221, v92
	v_add_f32_e32 v220, v220, v89
	v_mfma_f32_16x16x32_bf16 v[64:67], v[230:233], v[108:111], v[64:67]
	v_add_f32_e32 v221, v221, v93
	v_cvt_pk_bf16_f32 v244, v88, v89
	ds_read_b128 v[230:233], v246 offset:4096
	ds_write_b64 v184, v[146:147] offset:16384
	s_waitcnt lgkmcnt(13)
	v_mfma_f32_16x16x32_bf16 v[28:31], v[234:237], v[238:241], v[28:31]
	v_cvt_pk_bf16_f32 v245, v90, v91
	v_cvt_pk_bf16_f32 v206, v92, v93
	v_mfma_f32_16x16x32_bf16 v[24:27], v[234:237], v[216:219], v[24:27]
	v_cvt_pk_bf16_f32 v207, v94, v95
	ds_read_b128 v[234:237], v209 offset:63488
	global_load_dwordx4 v[148:151], v198, s[8:9]
	s_waitcnt lgkmcnt(13)
	v_mfma_f32_16x16x32_bf16 v[72:75], v[160:163], v[96:99], 0
	v_add_f32_e32 v220, v220, v90
	v_add_f32_e32 v221, v221, v94
	v_mfma_f32_16x16x32_bf16 v[76:79], v[160:163], v[112:115], 0
	v_add_f32_e32 v220, v220, v91
	v_add_f32_e32 v221, v221, v95
	ds_read_b128 v[160:163], v201 offset:8192
	global_load_dwordx4 v[144:147], v199, s[8:9]
	s_waitcnt lgkmcnt(13)
	v_mfma_f32_16x16x32_bf16 v[32:35], v[164:167], v[216:219], v[32:35]
	v_add_f32_e32 v194, v194, v220
	v_add_f32_e32 v195, v195, v221
	v_mfma_f32_16x16x32_bf16 v[36:39], v[164:167], v[238:241], v[36:39]
	v_exp_f32_e32 v64, v64
	ds_read_b128 v[164:167], v210 offset:49152
	global_load_dwordx4 v[136:139], v196, s[6:7]
	s_waitcnt lgkmcnt(12)
	v_mfma_f32_16x16x32_bf16 v[76:79], v[168:171], v[116:119], v[76:79]
	v_exp_f32_e32 v68, v68
	v_mfma_f32_16x16x32_bf16 v[72:75], v[168:171], v[100:103], v[72:75]
	v_exp_f32_e32 v65, v65
	ds_read_b128 v[168:171], v202 offset:8192
	global_load_dwordx4 v[140:143], v197, s[6:7]
	s_waitcnt lgkmcnt(11)
	v_mfma_f32_16x16x32_bf16 v[44:47], v[172:175], v[238:241], v[44:47]
	v_exp_f32_e32 v69, v69
	v_mfma_f32_16x16x32_bf16 v[40:43], v[172:175], v[216:219], v[40:43]
	v_exp_f32_e32 v66, v66
	ds_read_b128 v[172:175], v210 offset:51200
	s_waitcnt lgkmcnt(10)
	v_mfma_f32_16x16x32_bf16 v[72:75], v[176:179], v[104:107], v[72:75]
	v_exp_f32_e32 v70, v70
	v_mfma_f32_16x16x32_bf16 v[76:79], v[176:179], v[120:123], v[76:79]
	v_exp_f32_e32 v67, v67
	ds_read_b128 v[176:179], v203 offset:8192
	s_waitcnt lgkmcnt(9)
	v_mfma_f32_16x16x32_bf16 v[48:51], v[180:183], v[216:219], v[48:51]
	v_exp_f32_e32 v71, v71
	v_mfma_f32_16x16x32_bf16 v[52:55], v[180:183], v[238:241], v[52:55]
	v_add_f32_e32 v220, v64, v65
	ds_read_b128 v[180:183], v210 offset:53248
	s_waitcnt lgkmcnt(8)
	v_mfma_f32_16x16x32_bf16 v[76:79], v[230:233], v[124:127], v[76:79]
	v_add_f32_e32 v221, v68, v69
	v_mfma_f32_16x16x32_bf16 v[72:75], v[230:233], v[108:111], v[72:75]
	v_add_f32_e32 v220, v220, v66
	ds_read_b128 v[230:233], v246 offset:8192
	s_waitcnt lgkmcnt(7)
	v_mfma_f32_16x16x32_bf16 v[60:63], v[234:237], v[238:241], v[60:63]
	v_add_f32_e32 v221, v221, v70
	v_add_f32_e32 v220, v220, v67
	v_mfma_f32_16x16x32_bf16 v[56:59], v[234:237], v[216:219], v[56:59]
	v_add_f32_e32 v221, v221, v71
	ds_read_b128 v[234:237], v210 offset:55296
	s_waitcnt lgkmcnt(7)
	v_mfma_f32_16x16x32_bf16 v[80:83], v[160:163], v[96:99], 0
	v_exp_f32_e32 v72, v72
	v_mfma_f32_16x16x32_bf16 v[84:87], v[160:163], v[112:115], 0
	v_exp_f32_e32 v76, v76
	ds_read_b128 v[160:163], v201 offset:12288
	s_waitcnt lgkmcnt(7)
	v_mfma_f32_16x16x32_bf16 v[0:3], v[164:167], v[242:245], v[0:3]
	v_exp_f32_e32 v73, v73
	v_mfma_f32_16x16x32_bf16 v[4:7], v[164:167], v[204:207], v[4:7]
	v_exp_f32_e32 v77, v77
	ds_read_b128 v[164:167], v210 offset:57344
	s_waitcnt lgkmcnt(7)
	v_mfma_f32_16x16x32_bf16 v[84:87], v[168:171], v[116:119], v[84:87]
	v_exp_f32_e32 v74, v74
	v_mfma_f32_16x16x32_bf16 v[80:83], v[168:171], v[100:103], v[80:83]
	v_exp_f32_e32 v78, v78
	ds_read_b128 v[168:171], v202 offset:12288
	s_waitcnt lgkmcnt(7)
	v_mfma_f32_16x16x32_bf16 v[12:15], v[172:175], v[204:207], v[12:15]
	v_exp_f32_e32 v75, v75
	v_mfma_f32_16x16x32_bf16 v[8:11], v[172:175], v[242:245], v[8:11]
	v_exp_f32_e32 v79, v79
	ds_read_b128 v[172:175], v210 offset:59392
	s_waitcnt lgkmcnt(7)
	v_mfma_f32_16x16x32_bf16 v[80:83], v[176:179], v[104:107], v[80:83]
	v_add_f32_e32 v220, v220, v72
	v_add_f32_e32 v221, v221, v76
	v_mfma_f32_16x16x32_bf16 v[84:87], v[176:179], v[120:123], v[84:87]
	v_add_f32_e32 v220, v220, v73
	ds_read_b128 v[176:179], v203 offset:12288
	s_add_u32 s10, s10, 0x200
	s_addc_u32 s11, s11, 0
	s_add_u32 s12, s12, 0x40000
	s_addc_u32 s13, s13, 0
	s_add_i32 s4, s4, 4
	s_cmpk_lt_u32 s4, 0x104
	s_cselect_b64 s[6:7], -1, 0
	s_and_b64 s[6:7], s[0:1], s[6:7]
	s_and_b64 vcc, exec, s[6:7]
	s_waitcnt lgkmcnt(7)
	v_mfma_f32_16x16x32_bf16 v[16:19], v[180:183], v[242:245], v[16:19]
	v_add_f32_e32 v221, v221, v77
	v_add_f32_e32 v220, v220, v74
	v_mfma_f32_16x16x32_bf16 v[20:23], v[180:183], v[204:207], v[20:23]
	v_add_f32_e32 v221, v221, v78
	ds_read_b128 v[180:183], v210 offset:61440
	s_waitcnt lgkmcnt(7)
	v_mfma_f32_16x16x32_bf16 v[84:87], v[230:233], v[124:127], v[84:87]
	v_add_f32_e32 v220, v220, v75
	v_add_f32_e32 v221, v221, v79
	v_mfma_f32_16x16x32_bf16 v[80:83], v[230:233], v[108:111], v[80:83]
	v_cvt_pk_bf16_f32 v216, v64, v65
	ds_read_b128 v[230:233], v246 offset:12288
	s_waitcnt lgkmcnt(7)
	v_mfma_f32_16x16x32_bf16 v[28:31], v[234:237], v[204:207], v[28:31]
	v_cvt_pk_bf16_f32 v217, v66, v67
	v_cvt_pk_bf16_f32 v238, v68, v69
	v_mfma_f32_16x16x32_bf16 v[24:27], v[234:237], v[242:245], v[24:27]
	v_cvt_pk_bf16_f32 v239, v70, v71
	ds_read_b128 v[234:237], v210 offset:63488
	s_waitcnt lgkmcnt(7)
	v_mfma_f32_16x16x32_bf16 v[88:91], v[160:163], v[96:99], 0
	v_exp_f32_e32 v80, v80
	v_mfma_f32_16x16x32_bf16 v[92:95], v[160:163], v[112:115], 0
	v_exp_f32_e32 v84, v84
	s_waitcnt lgkmcnt(6)
	v_mfma_f32_16x16x32_bf16 v[32:35], v[164:167], v[242:245], v[32:35]
	v_exp_f32_e32 v81, v81
	v_mfma_f32_16x16x32_bf16 v[36:39], v[164:167], v[204:207], v[36:39]
	v_exp_f32_e32 v85, v85
	s_waitcnt lgkmcnt(5)
	v_mfma_f32_16x16x32_bf16 v[92:95], v[168:171], v[116:119], v[92:95]
	v_exp_f32_e32 v82, v82
	v_mfma_f32_16x16x32_bf16 v[88:91], v[168:171], v[100:103], v[88:91]
	v_exp_f32_e32 v86, v86
	s_waitcnt lgkmcnt(4)
	v_mfma_f32_16x16x32_bf16 v[44:47], v[172:175], v[204:207], v[44:47]
	v_exp_f32_e32 v83, v83
	v_mfma_f32_16x16x32_bf16 v[40:43], v[172:175], v[242:245], v[40:43]
	v_exp_f32_e32 v87, v87
	s_waitcnt lgkmcnt(3)
	v_mfma_f32_16x16x32_bf16 v[88:91], v[176:179], v[104:107], v[88:91]
	v_add_f32_e32 v220, v220, v80
	v_add_f32_e32 v221, v221, v84
	v_mfma_f32_16x16x32_bf16 v[92:95], v[176:179], v[120:123], v[92:95]
	v_add_f32_e32 v220, v220, v81
	s_waitcnt lgkmcnt(0)
	s_barrier
	ds_read_b128 v[160:163], v201 offset:16384
	ds_read_b128 v[164:167], v209 offset:0
	ds_read_b128 v[168:171], v202 offset:16384
	ds_read_b128 v[172:175], v209 offset:2048
	ds_read_b128 v[176:179], v203 offset:16384
	v_mfma_f32_16x16x32_bf16 v[48:51], v[180:183], v[242:245], v[48:51]
	v_add_f32_e32 v221, v221, v85
	v_add_f32_e32 v220, v220, v82
	v_mfma_f32_16x16x32_bf16 v[52:55], v[180:183], v[204:207], v[52:55]
	v_add_f32_e32 v221, v221, v86
	ds_read_b128 v[180:183], v209 offset:4096
	v_mfma_f32_16x16x32_bf16 v[92:95], v[230:233], v[124:127], v[92:95]
	v_add_f32_e32 v220, v220, v83
	v_add_f32_e32 v221, v221, v87
	v_mfma_f32_16x16x32_bf16 v[88:91], v[230:233], v[108:111], v[88:91]
	v_cvt_pk_bf16_f32 v218, v72, v73
	ds_read_b128 v[230:233], v246 offset:16384
	v_mfma_f32_16x16x32_bf16 v[60:63], v[234:237], v[204:207], v[60:63]
	v_cvt_pk_bf16_f32 v219, v74, v75
	v_cvt_pk_bf16_f32 v240, v76, v77
	v_mfma_f32_16x16x32_bf16 v[56:59], v[234:237], v[242:245], v[56:59]
	v_cvt_pk_bf16_f32 v241, v78, v79
	ds_read_b128 v[234:237], v209 offset:6144
	s_cbranch_vccnz .LBB0_734
	s_setprio 0
	s_waitcnt vmcnt(0)
	s_nop 7
	s_nop 7
	ds_swizzle_b32 v64, v194 offset:swizzle(SWAP,16)
	s_waitcnt lgkmcnt(0)
	v_add_f32_e32 v194, v194, v64
	v_mov_b32_e32 v65, v194
	s_nop 1
	v_permlane32_swap_b32_e32 v194, v65
	v_add_f32_e32 v194, v194, v65
	s_nop 0
	v_rcp_f32_e32 v66, v194
	ds_swizzle_b32 v64, v195 offset:swizzle(SWAP,16)
	s_waitcnt lgkmcnt(0)
	v_add_f32_e32 v195, v195, v64
	v_mov_b32_e32 v65, v195
	s_nop 1
	v_permlane32_swap_b32_e32 v195, v65
	v_add_f32_e32 v195, v195, v65
	s_nop 0
	v_rcp_f32_e32 v67, v195
	v_readlane_b32 s100, v250, 8
	v_mbcnt_lo_u32_b32 v68, -1, 0
	v_mbcnt_hi_u32_b32 v68, -1, v68
	v_and_b32_e32 v69, 15, v68
	v_lshrrev_b32_e32 v70, 4, v68
	s_lshr_b32 s101, s100, 1
	v_add_u32_e32 v69, s101, v69
	v_lshlrev_b32_e32 v69, 12, v69
	v_and_b32_e32 v71, 1, v70
	v_lshlrev_b32_e32 v71, 5, v71
	v_and_b32_e32 v70, 2, v70
	v_lshl_add_u32 v71, v70, 3, v71
	v_add_u32_e32 v70, v69, v71
	v_add_u32_e32 v71, 0x10000, v70
	v_mul_f32_e32 v0, v0, v66
	v_mul_f32_e32 v1, v1, v66
	v_mul_f32_e32 v2, v2, v66
	v_mul_f32_e32 v3, v3, v66
	v_mul_f32_e32 v8, v8, v66
	v_mul_f32_e32 v9, v9, v66
	v_mul_f32_e32 v10, v10, v66
	v_mul_f32_e32 v11, v11, v66
	v_cvt_pk_bf16_f32 v72, v0, v1
	v_cvt_pk_bf16_f32 v73, v2, v3
	v_cvt_pk_bf16_f32 v74, v8, v9
	v_cvt_pk_bf16_f32 v75, v10, v11
	s_nop 1
	v_permlane16_swap_b32_e32 v72, v74
	v_permlane16_swap_b32_e32 v73, v75
	s_nop 1
	global_store_dwordx4 v70, v[72:75], s[58:59] offset:0
	v_mul_f32_e32 v16, v16, v66
	v_mul_f32_e32 v17, v17, v66
	v_mul_f32_e32 v18, v18, v66
	v_mul_f32_e32 v19, v19, v66
	v_mul_f32_e32 v24, v24, v66
	v_mul_f32_e32 v25, v25, v66
	v_mul_f32_e32 v26, v26, v66
	v_mul_f32_e32 v27, v27, v66
	v_cvt_pk_bf16_f32 v76, v16, v17
	v_cvt_pk_bf16_f32 v77, v18, v19
	v_cvt_pk_bf16_f32 v78, v24, v25
	v_cvt_pk_bf16_f32 v79, v26, v27
	s_nop 1
	v_permlane16_swap_b32_e32 v76, v78
	v_permlane16_swap_b32_e32 v77, v79
	s_nop 1
	global_store_dwordx4 v70, v[76:79], s[58:59] offset:64
	v_mul_f32_e32 v32, v32, v66
	v_mul_f32_e32 v33, v33, v66
	v_mul_f32_e32 v34, v34, v66
	v_mul_f32_e32 v35, v35, v66
	v_mul_f32_e32 v40, v40, v66
	v_mul_f32_e32 v41, v41, v66
	v_mul_f32_e32 v42, v42, v66
	v_mul_f32_e32 v43, v43, v66
	v_cvt_pk_bf16_f32 v80, v32, v33
	v_cvt_pk_bf16_f32 v81, v34, v35
	v_cvt_pk_bf16_f32 v82, v40, v41
	v_cvt_pk_bf16_f32 v83, v42, v43
	s_nop 1
	v_permlane16_swap_b32_e32 v80, v82
	v_permlane16_swap_b32_e32 v81, v83
	s_nop 1
	global_store_dwordx4 v70, v[80:83], s[58:59] offset:128
	v_mul_f32_e32 v48, v48, v66
	v_mul_f32_e32 v49, v49, v66
	v_mul_f32_e32 v50, v50, v66
	v_mul_f32_e32 v51, v51, v66
	v_mul_f32_e32 v56, v56, v66
	v_mul_f32_e32 v57, v57, v66
	v_mul_f32_e32 v58, v58, v66
	v_mul_f32_e32 v59, v59, v66
	v_cvt_pk_bf16_f32 v84, v48, v49
	v_cvt_pk_bf16_f32 v85, v50, v51
	v_cvt_pk_bf16_f32 v86, v56, v57
	v_cvt_pk_bf16_f32 v87, v58, v59
	s_nop 1
	v_permlane16_swap_b32_e32 v84, v86
	v_permlane16_swap_b32_e32 v85, v87
	s_nop 1
	global_store_dwordx4 v70, v[84:87], s[58:59] offset:192
	v_mul_f32_e32 v4, v4, v67
	v_mul_f32_e32 v5, v5, v67
	v_mul_f32_e32 v6, v6, v67
	v_mul_f32_e32 v7, v7, v67
	v_mul_f32_e32 v12, v12, v67
	v_mul_f32_e32 v13, v13, v67
	v_mul_f32_e32 v14, v14, v67
	v_mul_f32_e32 v15, v15, v67
	v_cvt_pk_bf16_f32 v88, v4, v5
	v_cvt_pk_bf16_f32 v89, v6, v7
	v_cvt_pk_bf16_f32 v90, v12, v13
	v_cvt_pk_bf16_f32 v91, v14, v15
	s_nop 1
	v_permlane16_swap_b32_e32 v88, v90
	v_permlane16_swap_b32_e32 v89, v91
	s_nop 1
	global_store_dwordx4 v71, v[88:91], s[58:59] offset:0
	v_mul_f32_e32 v20, v20, v67
	v_mul_f32_e32 v21, v21, v67
	v_mul_f32_e32 v22, v22, v67
	v_mul_f32_e32 v23, v23, v67
	v_mul_f32_e32 v28, v28, v67
	v_mul_f32_e32 v29, v29, v67
	v_mul_f32_e32 v30, v30, v67
	v_mul_f32_e32 v31, v31, v67
	v_cvt_pk_bf16_f32 v92, v20, v21
	v_cvt_pk_bf16_f32 v93, v22, v23
	v_cvt_pk_bf16_f32 v94, v28, v29
	v_cvt_pk_bf16_f32 v95, v30, v31
	s_nop 1
	v_permlane16_swap_b32_e32 v92, v94
	v_permlane16_swap_b32_e32 v93, v95
	s_nop 1
	global_store_dwordx4 v71, v[92:95], s[58:59] offset:64
	v_mul_f32_e32 v36, v36, v67
	v_mul_f32_e32 v37, v37, v67
	v_mul_f32_e32 v38, v38, v67
	v_mul_f32_e32 v39, v39, v67
	v_mul_f32_e32 v44, v44, v67
	v_mul_f32_e32 v45, v45, v67
	v_mul_f32_e32 v46, v46, v67
	v_mul_f32_e32 v47, v47, v67
	v_cvt_pk_bf16_f32 v72, v36, v37
	v_cvt_pk_bf16_f32 v73, v38, v39
	v_cvt_pk_bf16_f32 v74, v44, v45
	v_cvt_pk_bf16_f32 v75, v46, v47
	s_nop 1
	v_permlane16_swap_b32_e32 v72, v74
	v_permlane16_swap_b32_e32 v73, v75
	s_nop 1
	global_store_dwordx4 v71, v[72:75], s[58:59] offset:128
	v_mul_f32_e32 v52, v52, v67
	v_mul_f32_e32 v53, v53, v67
	v_mul_f32_e32 v54, v54, v67
	v_mul_f32_e32 v55, v55, v67
	v_mul_f32_e32 v60, v60, v67
	v_mul_f32_e32 v61, v61, v67
	v_mul_f32_e32 v62, v62, v67
	v_mul_f32_e32 v63, v63, v67
	v_cvt_pk_bf16_f32 v76, v52, v53
	v_cvt_pk_bf16_f32 v77, v54, v55
	v_cvt_pk_bf16_f32 v78, v60, v61
	v_cvt_pk_bf16_f32 v79, v62, v63
	s_nop 1
	v_permlane16_swap_b32_e32 v76, v78
	v_permlane16_swap_b32_e32 v77, v79
	s_nop 1
	global_store_dwordx4 v71, v[76:79], s[58:59] offset:192
	s_barrier
